# speedup vs baseline: 1.0078x; 1.0078x over previous
.LBB1_235:
	v_subrev_u32_e32 v0, 0x100, v0
	s_movk_i32 s0, 0xf0
	v_cmp_gt_u32_e32 vcc, s0, v0
	s_and_saveexec_b64 s[0:1], vcc
	s_cbranch_execz .Lepi_idle
	s_load_dwordx4 s[68:71], s[14:15], 0x0
	s_load_dwordx2 s[72:73], s[14:15], 0x10
	s_movk_i32 s0, 0x77
	v_mov_b32_e32 v1, 0xffffff88
	v_cmp_lt_u32_e32 vcc, s0, v0
	v_mov_b32_e32 v2, 0x44704000
	s_mov_b32 s0, 0xf800000
	v_cndmask_b32_e32 v1, 0, v1, vcc
	v_add_u32_e32 v0, v1, v0
	v_cvt_f32_u32_e32 v1, v0
	s_mov_b32 s5, 0x17800
	s_mov_b32 s4, 0x3eb17218
	v_fmac_f32_e32 v2, 0xc1000000, v1
	v_sqrt_f32_e32 v1, v2
	s_nop 0
	v_sub_f32_e32 v1, 0x41f80000, v1
	v_mul_f32_e32 v1, 0.5, v1
	v_cvt_i32_f32_e32 v1, v1
	s_and_b64 s[0:1], exec, s[16:17]
	s_cselect_b32 s2, s40, s38
	s_cselect_b32 s3, s39, s33
	v_sub_u32_e32 v2, 31, v1
	v_mul_lo_u32 v2, v2, v1
	v_lshrrev_b32_e32 v3, 31, v2
	v_add_u32_e32 v2, v2, v3
	v_ashrrev_i32_e32 v2, 1, v2
	v_cmp_gt_i32_e64 s[0:1], v2, v0
	s_nop 1
	v_subbrev_co_u32_e64 v1, s[0:1], 0, v1, s[0:1]
	v_add_u32_e32 v2, 1, v1
	v_sub_u32_e32 v3, 30, v1
	v_mul_lo_u32 v3, v2, v3
	v_lshrrev_b32_e32 v4, 31, v3
	v_add_u32_e32 v3, v3, v4
	v_ashrrev_i32_e32 v3, 1, v3
	v_cmp_gt_i32_e64 s[0:1], v3, v0
	s_nop 1
	v_cndmask_b32_e64 v12, v2, v1, s[0:1]
	v_sub_u32_e32 v1, 31, v12
	v_mul_lo_u32 v1, v1, v12
	v_lshrrev_b32_e32 v2, 31, v1
	v_add_u32_e32 v1, v1, v2
	v_ashrrev_i32_e32 v1, 1, v1
	v_sub_u32_e32 v0, v0, v1
	v_cndmask_b32_e64 v1, 0, 16, vcc
	v_lshl_or_b32 v1, s2, 5, v1
	v_add_u32_e32 v1, v1, v12
	v_sub_u32_e32 v2, 0xff, v1
	v_mul_lo_u32 v1, v2, v1
	v_lshrrev_b32_e32 v2, 31, v1
	v_add_u32_e32 v1, v1, v2
	v_ashrrev_i32_e32 v1, 1, v1
	v_add3_u32 v13, v12, v0, 1
	v_add_u32_e32 v0, v1, v0
	v_ashrrev_i32_e32 v1, 31, v0
	v_mov_b32_e32 v2, 0x1fc0
	v_mad_u64_u32 v[0:1], s[0:1], s3, v2, v[0:1]
	v_mad_u64_u32 v[4:5], s[0:1], v0, 24, s[10:11]
	v_mov_b32_e32 v0, 0x17800
	v_lshl_add_u32 v14, v12, 2, v0
	v_mov_b32_e32 v0, 0x60
	v_cndmask_b32_e32 v15, 0, v0, vcc
	v_or_b32_e32 v2, 16, v15
	v_add_lshl_u32 v3, v2, v12, 6
	v_add_u32_e32 v2, v2, v13
	v_lshl_add_u32 v6, v2, 6, v14
	v_add_u32_e32 v2, 32, v15
	v_add_lshl_u32 v7, v2, v12, 6
	v_add_u32_e32 v2, v2, v13
	v_lshl_add_u32 v8, v2, 6, v14
	v_add_u32_e32 v2, 48, v15
	v_mad_i32_i24 v5, v1, 24, v5
	v_add_lshl_u32 v0, v15, v12, 6
	v_lshlrev_b32_e32 v16, 2, v13
	v_add_u32_e32 v1, v15, v13
	v_add_lshl_u32 v9, v2, v12, 6
	v_add_u32_e32 v17, 64, v15
	v_add_u32_e32 v15, 0x50, v15
	v_add3_u32 v0, v0, v16, s5
	v_lshl_add_u32 v1, v1, 6, v14
	v_add3_u32 v3, v3, v16, s5
	v_add3_u32 v7, v7, v16, s5
	v_add3_u32 v9, v9, v16, s5
	v_add_u32_e32 v2, v2, v13
	v_add_lshl_u32 v18, v17, v12, 6
	v_add_lshl_u32 v12, v15, v12, 6
	v_lshl_add_u32 v10, v2, 6, v14
	ds_read_b32 v0, v0
	ds_read_b32 v2, v1
	ds_read_b32 v1, v3
	ds_read_b32 v3, v6
	ds_read_b32 v6, v7
	ds_read_b32 v8, v8
	ds_read_b32 v7, v9
	ds_read_b32 v9, v10
	v_add3_u32 v18, v18, v16, s5
	v_add3_u32 v16, v12, v16, s5
	v_add_u32_e32 v12, v15, v13
	v_add_u32_e32 v17, v17, v13
	v_lshl_add_u32 v15, v12, 6, v14
	v_lshl_add_u32 v17, v17, 6, v14
	ds_read_b32 v12, v18
	ds_read_b32 v14, v17
	ds_read_b32 v13, v16
	ds_read_b32 v15, v15
	s_waitcnt lgkmcnt(0)
	v_pk_add_f32 v[0:1], v[0:1], v[2:3]
	v_mov_b32_e32 v2, s70
	v_mov_b32_e32 v3, s71
	v_mov_b64_e32 v[10:11], s[68:69]
	v_pk_add_f32 v[6:7], v[6:7], v[8:9]
	v_pk_fma_f32 v[0:1], v[0:1], s[4:5], v[10:11] op_sel_hi:[1,0,1]
	v_pk_fma_f32 v[2:3], v[6:7], s[4:5], v[2:3] op_sel_hi:[1,0,1]
	global_store_dwordx4 v[4:5], v[0:3], off
	s_nop 1
	v_pk_add_f32 v[0:1], v[12:13], v[14:15]
	v_mov_b64_e32 v[2:3], s[72:73]
	v_pk_fma_f32 v[0:1], v[0:1], s[4:5], v[2:3] op_sel_hi:[1,0,1]
	global_store_dwordx2 v[4:5], v[0:1], off offset:16
	s_endpgm
